# s10p + DeltaNet chunk-local q/k/v LDS tile fill (12 chunks) issues all loads before counted-vmcnt LDS writes, L0 and L1; padded to 256B multiples
# speedup vs baseline: 1.0060x; 1.0060x over previous
; #define LAS __attribute__((address_space(3)))
; template <int NW> DI void dn1_unit(const Params& P, const Frame& F, int cidx) {
;     ...
;     for (int id = F.tid; id < 3072; id += NT) { const int which = id >> 10, rem = id & 1023, row = rem >> 4, ch = rem & 15;
;         *(LAS u32x4*)(Qs + which * 17408 + row * 272 + ch * 16) = *(const u32x4*)(ZC + (r0 + row) * 2560 + which * 512 + h * 128 + ch * 8); }
.LBB0_385:
	v_and_b32_e32 v61, 63, v0
	v_or_b32_e32 v11, s34, v61
	v_mov_b64_e32 v[2:3], s[30:31]
	s_movk_i32 s60, 0x1400
	s_mul_i32 s36, s35, 0x1400
	v_mad_u64_u32 v[2:3], s[82:83], v11, s60, v[2:3]
	v_add_u32_e32 v3, s36, v3
	v_and_b32_e32 v14, 0xfffffc00, v1
	v_lshl_add_u64 v[2:3], v[2:3], 0, v[14:15]
	s_lshl_b32 s36, s61, 1
	v_lshl_add_u64 v[2:3], v[2:3], 0, s[36:37]
	v_mov_b32_e32 v11, v15
	v_lshl_add_u64 v[2:3], v[2:3], 0, v[10:11]
	global_load_dwordx4 v[186:189], v[2:3], off
	v_lshrrev_b32_e32 v60, 10, v1
	v_mov_b32_e32 v2, s28
	s_movk_i32 s60, 0x4400
	v_mad_u32_u24 v2, v60, s60, v2
	v_mul_u32_u24_e32 v3, 0x110, v61
	v_add3_u32 v234, v2, v3, v6
	v_add_u32_e32 v0, 16, v0
	v_add_u32_e32 v1, 0x100, v1
	v_and_b32_e32 v61, 63, v0
	v_or_b32_e32 v11, s34, v61
	v_mov_b64_e32 v[2:3], s[30:31]
	s_movk_i32 s60, 0x1400
	s_mul_i32 s36, s35, 0x1400
	v_mad_u64_u32 v[2:3], s[82:83], v11, s60, v[2:3]
	v_add_u32_e32 v3, s36, v3
	v_and_b32_e32 v14, 0xfffffc00, v1
	v_lshl_add_u64 v[2:3], v[2:3], 0, v[14:15]
	s_lshl_b32 s36, s61, 1
	v_lshl_add_u64 v[2:3], v[2:3], 0, s[36:37]
	v_mov_b32_e32 v11, v15
	v_lshl_add_u64 v[2:3], v[2:3], 0, v[10:11]
	global_load_dwordx4 v[190:193], v[2:3], off
	v_lshrrev_b32_e32 v60, 10, v1
	v_mov_b32_e32 v2, s28
	s_movk_i32 s60, 0x4400
	v_mad_u32_u24 v2, v60, s60, v2
	v_mul_u32_u24_e32 v3, 0x110, v61
	v_add3_u32 v235, v2, v3, v6
	v_add_u32_e32 v0, 16, v0
	v_add_u32_e32 v1, 0x100, v1
	v_and_b32_e32 v61, 63, v0
	v_or_b32_e32 v11, s34, v61
	v_mov_b64_e32 v[2:3], s[30:31]
	s_movk_i32 s60, 0x1400
	s_mul_i32 s36, s35, 0x1400
	v_mad_u64_u32 v[2:3], s[82:83], v11, s60, v[2:3]
	v_add_u32_e32 v3, s36, v3
	v_and_b32_e32 v14, 0xfffffc00, v1
	v_lshl_add_u64 v[2:3], v[2:3], 0, v[14:15]
	s_lshl_b32 s36, s61, 1
	v_lshl_add_u64 v[2:3], v[2:3], 0, s[36:37]
	v_mov_b32_e32 v11, v15
	v_lshl_add_u64 v[2:3], v[2:3], 0, v[10:11]
	global_load_dwordx4 v[194:197], v[2:3], off
	v_lshrrev_b32_e32 v60, 10, v1
	v_mov_b32_e32 v2, s28
	s_movk_i32 s60, 0x4400
	v_mad_u32_u24 v2, v60, s60, v2
	v_mul_u32_u24_e32 v3, 0x110, v61
	v_add3_u32 v236, v2, v3, v6
	v_add_u32_e32 v0, 16, v0
	v_add_u32_e32 v1, 0x100, v1
	v_and_b32_e32 v61, 63, v0
	v_or_b32_e32 v11, s34, v61
	v_mov_b64_e32 v[2:3], s[30:31]
	s_movk_i32 s60, 0x1400
	s_mul_i32 s36, s35, 0x1400
	v_mad_u64_u32 v[2:3], s[82:83], v11, s60, v[2:3]
	v_add_u32_e32 v3, s36, v3
	v_and_b32_e32 v14, 0xfffffc00, v1
	v_lshl_add_u64 v[2:3], v[2:3], 0, v[14:15]
	s_lshl_b32 s36, s61, 1
	v_lshl_add_u64 v[2:3], v[2:3], 0, s[36:37]
	v_mov_b32_e32 v11, v15
	v_lshl_add_u64 v[2:3], v[2:3], 0, v[10:11]
	global_load_dwordx4 v[198:201], v[2:3], off
	v_lshrrev_b32_e32 v60, 10, v1
	v_mov_b32_e32 v2, s28
	s_movk_i32 s60, 0x4400
	v_mad_u32_u24 v2, v60, s60, v2
	v_mul_u32_u24_e32 v3, 0x110, v61
	v_add3_u32 v237, v2, v3, v6
	v_add_u32_e32 v0, 16, v0
	v_add_u32_e32 v1, 0x100, v1
	v_and_b32_e32 v61, 63, v0
	v_or_b32_e32 v11, s34, v61
	v_mov_b64_e32 v[2:3], s[30:31]
	s_movk_i32 s60, 0x1400
	s_mul_i32 s36, s35, 0x1400
	v_mad_u64_u32 v[2:3], s[82:83], v11, s60, v[2:3]
	v_add_u32_e32 v3, s36, v3
	v_and_b32_e32 v14, 0xfffffc00, v1
	v_lshl_add_u64 v[2:3], v[2:3], 0, v[14:15]
	s_lshl_b32 s36, s61, 1
	v_lshl_add_u64 v[2:3], v[2:3], 0, s[36:37]
	v_mov_b32_e32 v11, v15
	v_lshl_add_u64 v[2:3], v[2:3], 0, v[10:11]
	global_load_dwordx4 v[202:205], v[2:3], off
	v_lshrrev_b32_e32 v60, 10, v1
	v_mov_b32_e32 v2, s28
	s_movk_i32 s60, 0x4400
	v_mad_u32_u24 v2, v60, s60, v2
	v_mul_u32_u24_e32 v3, 0x110, v61
	v_add3_u32 v238, v2, v3, v6
	v_add_u32_e32 v0, 16, v0
	v_add_u32_e32 v1, 0x100, v1
	v_and_b32_e32 v61, 63, v0
	v_or_b32_e32 v11, s34, v61
	v_mov_b64_e32 v[2:3], s[30:31]
	s_movk_i32 s60, 0x1400
	s_mul_i32 s36, s35, 0x1400
	v_mad_u64_u32 v[2:3], s[82:83], v11, s60, v[2:3]
	v_add_u32_e32 v3, s36, v3
	v_and_b32_e32 v14, 0xfffffc00, v1
	v_lshl_add_u64 v[2:3], v[2:3], 0, v[14:15]
	s_lshl_b32 s36, s61, 1
	v_lshl_add_u64 v[2:3], v[2:3], 0, s[36:37]
	v_mov_b32_e32 v11, v15
	v_lshl_add_u64 v[2:3], v[2:3], 0, v[10:11]
	global_load_dwordx4 v[206:209], v[2:3], off
	v_lshrrev_b32_e32 v60, 10, v1
	v_mov_b32_e32 v2, s28
	s_movk_i32 s60, 0x4400
	v_mad_u32_u24 v2, v60, s60, v2
	v_mul_u32_u24_e32 v3, 0x110, v61
	v_add3_u32 v239, v2, v3, v6
	v_add_u32_e32 v0, 16, v0
	v_add_u32_e32 v1, 0x100, v1
	v_and_b32_e32 v61, 63, v0
	v_or_b32_e32 v11, s34, v61
	v_mov_b64_e32 v[2:3], s[30:31]
	s_movk_i32 s60, 0x1400
	s_mul_i32 s36, s35, 0x1400
	v_mad_u64_u32 v[2:3], s[82:83], v11, s60, v[2:3]
	v_add_u32_e32 v3, s36, v3
	v_and_b32_e32 v14, 0xfffffc00, v1
	v_lshl_add_u64 v[2:3], v[2:3], 0, v[14:15]
	s_lshl_b32 s36, s61, 1
	v_lshl_add_u64 v[2:3], v[2:3], 0, s[36:37]
	v_mov_b32_e32 v11, v15
	v_lshl_add_u64 v[2:3], v[2:3], 0, v[10:11]
	global_load_dwordx4 v[210:213], v[2:3], off
	v_lshrrev_b32_e32 v60, 10, v1
	v_mov_b32_e32 v2, s28
	s_movk_i32 s60, 0x4400
	v_mad_u32_u24 v2, v60, s60, v2
	v_mul_u32_u24_e32 v3, 0x110, v61
	v_add3_u32 v240, v2, v3, v6
	v_add_u32_e32 v0, 16, v0
	v_add_u32_e32 v1, 0x100, v1
	v_and_b32_e32 v61, 63, v0
	v_or_b32_e32 v11, s34, v61
	v_mov_b64_e32 v[2:3], s[30:31]
	s_movk_i32 s60, 0x1400
	s_mul_i32 s36, s35, 0x1400
	v_mad_u64_u32 v[2:3], s[82:83], v11, s60, v[2:3]
	v_add_u32_e32 v3, s36, v3
	v_and_b32_e32 v14, 0xfffffc00, v1
	v_lshl_add_u64 v[2:3], v[2:3], 0, v[14:15]
	s_lshl_b32 s36, s61, 1
	v_lshl_add_u64 v[2:3], v[2:3], 0, s[36:37]
	v_mov_b32_e32 v11, v15
; #define LAS __attribute__((address_space(3)))
; template <int NW> DI void dn1_unit(const Params& P, const Frame& F, int cidx) {
;     ...
;     for (int id = F.tid; id < 3072; id += NT) { const int which = id >> 10, rem = id & 1023, row = rem >> 4, ch = rem & 15;
;         *(LAS u32x4*)(Qs + which * 17408 + row * 272 + ch * 16) = *(const u32x4*)(ZC + (r0 + row) * 2560 + which * 512 + h * 128 + ch * 8); }
;     if (F.tid < 64) { bts[F.tid] = GD[(r0 + F.tid) * 16 + h]; const float gc = wave_incl_sum(GD[(r0 + F.tid) * 16 + 4 + h], lane); gcs[F.tid] = gc;
;         if (lane == 63) ((float*)(ws + WS_DNGL))[cidx] = __expf(gc); }
	v_lshl_add_u64 v[2:3], v[2:3], 0, v[10:11]
	global_load_dwordx4 v[214:217], v[2:3], off
	v_lshrrev_b32_e32 v60, 10, v1
	v_mov_b32_e32 v2, s28
	s_movk_i32 s60, 0x4400
	v_mad_u32_u24 v2, v60, s60, v2
	v_mul_u32_u24_e32 v3, 0x110, v61
	v_add3_u32 v241, v2, v3, v6
	v_add_u32_e32 v0, 16, v0
	v_add_u32_e32 v1, 0x100, v1
	v_and_b32_e32 v61, 63, v0
	v_or_b32_e32 v11, s34, v61
	v_mov_b64_e32 v[2:3], s[30:31]
	s_movk_i32 s60, 0x1400
	s_mul_i32 s36, s35, 0x1400
	v_mad_u64_u32 v[2:3], s[82:83], v11, s60, v[2:3]
	v_add_u32_e32 v3, s36, v3
	v_and_b32_e32 v14, 0xfffffc00, v1
	v_lshl_add_u64 v[2:3], v[2:3], 0, v[14:15]
	s_lshl_b32 s36, s61, 1
	v_lshl_add_u64 v[2:3], v[2:3], 0, s[36:37]
	v_mov_b32_e32 v11, v15
	v_lshl_add_u64 v[2:3], v[2:3], 0, v[10:11]
	global_load_dwordx4 v[218:221], v[2:3], off
	v_lshrrev_b32_e32 v60, 10, v1
	v_mov_b32_e32 v2, s28
	s_movk_i32 s60, 0x4400
	v_mad_u32_u24 v2, v60, s60, v2
	v_mul_u32_u24_e32 v3, 0x110, v61
	v_add3_u32 v242, v2, v3, v6
	v_add_u32_e32 v0, 16, v0
	v_add_u32_e32 v1, 0x100, v1
	v_and_b32_e32 v61, 63, v0
	v_or_b32_e32 v11, s34, v61
	v_mov_b64_e32 v[2:3], s[30:31]
	s_movk_i32 s60, 0x1400
	s_mul_i32 s36, s35, 0x1400
	v_mad_u64_u32 v[2:3], s[82:83], v11, s60, v[2:3]
	v_add_u32_e32 v3, s36, v3
	v_and_b32_e32 v14, 0xfffffc00, v1
	v_lshl_add_u64 v[2:3], v[2:3], 0, v[14:15]
	s_lshl_b32 s36, s61, 1
	v_lshl_add_u64 v[2:3], v[2:3], 0, s[36:37]
	v_mov_b32_e32 v11, v15
	v_lshl_add_u64 v[2:3], v[2:3], 0, v[10:11]
	global_load_dwordx4 v[222:225], v[2:3], off
	v_lshrrev_b32_e32 v60, 10, v1
	v_mov_b32_e32 v2, s28
	s_movk_i32 s60, 0x4400
	v_mad_u32_u24 v2, v60, s60, v2
	v_mul_u32_u24_e32 v3, 0x110, v61
	v_add3_u32 v243, v2, v3, v6
	v_add_u32_e32 v0, 16, v0
	v_add_u32_e32 v1, 0x100, v1
	v_and_b32_e32 v61, 63, v0
	v_or_b32_e32 v11, s34, v61
	v_mov_b64_e32 v[2:3], s[30:31]
	s_movk_i32 s60, 0x1400
	s_mul_i32 s36, s35, 0x1400
	v_mad_u64_u32 v[2:3], s[82:83], v11, s60, v[2:3]
	v_add_u32_e32 v3, s36, v3
	v_and_b32_e32 v14, 0xfffffc00, v1
	v_lshl_add_u64 v[2:3], v[2:3], 0, v[14:15]
	s_lshl_b32 s36, s61, 1
	v_lshl_add_u64 v[2:3], v[2:3], 0, s[36:37]
	v_mov_b32_e32 v11, v15
	v_lshl_add_u64 v[2:3], v[2:3], 0, v[10:11]
	global_load_dwordx4 v[226:229], v[2:3], off
	v_lshrrev_b32_e32 v60, 10, v1
	v_mov_b32_e32 v2, s28
	s_movk_i32 s60, 0x4400
	v_mad_u32_u24 v2, v60, s60, v2
	v_mul_u32_u24_e32 v3, 0x110, v61
	v_add3_u32 v244, v2, v3, v6
	v_add_u32_e32 v0, 16, v0
	v_add_u32_e32 v1, 0x100, v1
	v_and_b32_e32 v61, 63, v0
	v_or_b32_e32 v11, s34, v61
	v_mov_b64_e32 v[2:3], s[30:31]
	s_movk_i32 s60, 0x1400
	s_mul_i32 s36, s35, 0x1400
	v_mad_u64_u32 v[2:3], s[82:83], v11, s60, v[2:3]
	v_add_u32_e32 v3, s36, v3
	v_and_b32_e32 v14, 0xfffffc00, v1
	v_lshl_add_u64 v[2:3], v[2:3], 0, v[14:15]
	s_lshl_b32 s36, s61, 1
	v_lshl_add_u64 v[2:3], v[2:3], 0, s[36:37]
	v_mov_b32_e32 v11, v15
	v_lshl_add_u64 v[2:3], v[2:3], 0, v[10:11]
	global_load_dwordx4 v[230:233], v[2:3], off
	v_lshrrev_b32_e32 v60, 10, v1
	v_mov_b32_e32 v2, s28
	s_movk_i32 s60, 0x4400
	v_mad_u32_u24 v2, v60, s60, v2
	v_mul_u32_u24_e32 v3, 0x110, v61
	v_add3_u32 v245, v2, v3, v6
	s_waitcnt vmcnt(11)
	ds_write_b128 v234, v[186:189] offset:16896
	s_waitcnt vmcnt(10)
	ds_write_b128 v235, v[190:193] offset:16896
	s_waitcnt vmcnt(9)
	ds_write_b128 v236, v[194:197] offset:16896
	s_waitcnt vmcnt(8)
	ds_write_b128 v237, v[198:201] offset:16896
	s_waitcnt vmcnt(7)
	ds_write_b128 v238, v[202:205] offset:16896
	s_waitcnt vmcnt(6)
	ds_write_b128 v239, v[206:209] offset:16896
	s_waitcnt vmcnt(5)
	ds_write_b128 v240, v[210:213] offset:16896
	s_waitcnt vmcnt(4)
	ds_write_b128 v241, v[214:217] offset:16896
	s_waitcnt vmcnt(3)
	ds_write_b128 v242, v[218:221] offset:16896
	s_waitcnt vmcnt(2)
	ds_write_b128 v243, v[222:225] offset:16896
	s_waitcnt vmcnt(1)
	ds_write_b128 v244, v[226:229] offset:16896
	s_waitcnt vmcnt(0)
	ds_write_b128 v245, v[230:233] offset:16896
	s_or_b64 exec, exec, s[24:25]
	s_lshl_b32 s60, s27, 5
	s_or_b32 s24, s60, s93
	s_and_saveexec_b64 s[82:83], s[4:5]
	s_cbranch_execz .LBB0_389
	s_lshl_b32 s26, s26, 2
	s_mov_b32 s27, s37
	v_lshl_add_u64 v[0:1], v[8:9], 0, s[26:27]
	global_load_dword v2, v[0:1], off offset:16
	s_nop 0
	global_load_dword v1, v[0:1], off
	v_readlane_b32 s26, v255, 0
	v_readlane_b32 s27, v255, 1
	s_waitcnt vmcnt(1)
	ds_bpermute_b32 v0, v62, v2
	s_waitcnt lgkmcnt(0)
	v_add_f32_e32 v0, v2, v0
	v_cndmask_b32_e64 v0, v0, v2, s[6:7]
	ds_bpermute_b32 v2, v63, v0
	s_waitcnt lgkmcnt(0)
	v_add_f32_e32 v2, v0, v2
	v_cndmask_b32_e64 v0, v2, v0, s[8:9]
	ds_bpermute_b32 v2, v64, v0
	s_waitcnt lgkmcnt(0)
	v_add_f32_e32 v2, v0, v2
	v_cndmask_b32_e64 v0, v2, v0, s[10:11]
	ds_bpermute_b32 v2, v65, v0
	s_waitcnt lgkmcnt(0)
	v_add_f32_e32 v2, v0, v2
	v_cndmask_b32_e64 v0, v2, v0, s[12:13]
	ds_bpermute_b32 v2, v66, v0
	s_waitcnt lgkmcnt(0)
	v_add_f32_e32 v2, v0, v2
	v_cndmask_b32_e64 v2, v2, v0, s[14:15]
	ds_bpermute_b32 v0, v67, v2
	s_waitcnt lgkmcnt(0)
	v_add_f32_e32 v0, v2, v0
	v_cndmask_b32_e64 v2, v0, v2, s[16:17]
	s_waitcnt vmcnt(0)
	ds_write2st64_b32 v72, v2, v1 offset0:64 offset1:65
	s_and_b64 exec, exec, s[26:27]
	s_cbranch_execz .LBB0_389
	v_mul_f32_e32 v0, 0x3fb8aa3b, v0
	s_ashr_i32 s25, s24, 31
	v_exp_f32_e32 v0, v0
	s_lshl_b64 s[26:27], s[24:25], 2
	v_readlane_b32 s25, v255, 2
	s_add_u32 s26, s25, s26
	v_readlane_b32 s25, v255, 3
	s_addc_u32 s27, s25, s27
	global_store_dword v15, v0, s[26:27]

.LBB0_1017:
	s_cmp_lt_u32 s3, 0x40001
	s_mov_b64 s[18:19], 0
	s_cselect_b64 s[20:21], -1, 0
	s_mov_b64 s[22:23], -1
	s_and_b64 vcc, exec, s[20:21]
	s_cbranch_vccnz .LBB0_1014
	s_branch .LBB0_1011
	s_nop 0
	s_nop 0
	s_nop 0
	s_nop 0
	s_nop 0
	s_nop 0
	s_nop 0
	s_nop 0
	s_nop 0
	s_nop 0
	s_nop 0
	s_nop 0
	s_nop 0
	s_nop 0
	s_nop 0
	s_nop 0
	s_nop 0
	s_nop 0
	s_nop 0
	s_nop 0
	s_nop 0
	s_nop 0
	s_nop 0
	s_nop 0
	s_nop 0
	s_nop 0
	s_nop 0
	s_nop 0
	s_nop 0
	s_nop 0
	s_nop 0
	s_nop 0
	s_nop 0
	s_nop 0
	s_nop 0
	s_nop 0
	s_nop 0
	s_nop 0
	s_nop 0
	s_nop 0
	s_nop 0
	s_nop 0
	s_nop 0
	s_nop 0
	s_nop 0
	s_nop 0
	s_nop 0
	s_nop 0
	s_nop 0
	s_nop 0
	s_nop 0
	s_nop 0
	s_nop 0
	s_nop 0
	s_nop 0
	s_nop 0
	s_nop 0
	s_nop 0
	s_nop 0
	s_nop 0
	s_nop 0

; #define LAS __attribute__((address_space(3)))
; template <int NW> DI void dn1_unit(const Params& P, const Frame& F, int cidx) {
;     ...
;     for (int id = F.tid; id < 3072; id += NT) { const int which = id >> 10, rem = id & 1023, row = rem >> 4, ch = rem & 15;
;         *(LAS u32x4*)(Qs + which * 17408 + row * 272 + ch * 16) = *(const u32x4*)(ZC + (r0 + row) * 2560 + which * 512 + h * 128 + ch * 8); }
.LBB0_1950:
	v_and_b32_e32 v61, 63, v0
	v_or_b32_e32 v11, s26, v61
	v_mov_b64_e32 v[2:3], s[24:25]
	s_movk_i32 s82, 0x1400
	s_mul_i32 s28, s27, 0x1400
	v_mad_u64_u32 v[2:3], s[82:83], v11, s82, v[2:3]
	v_add_u32_e32 v3, s28, v3
	v_and_b32_e32 v14, 0xfffffc00, v1
	v_lshl_add_u64 v[2:3], v[2:3], 0, v[14:15]
	s_lshl_b32 s28, s97, 1
	v_lshl_add_u64 v[2:3], v[2:3], 0, s[28:29]
	v_mov_b32_e32 v11, v15
	v_lshl_add_u64 v[2:3], v[2:3], 0, v[10:11]
	global_load_dwordx4 v[186:189], v[2:3], off
	v_lshrrev_b32_e32 v60, 10, v1
	v_mov_b32_e32 v2, s0
	s_movk_i32 s82, 0x4400
	v_mad_u32_u24 v2, v60, s82, v2
	v_mul_u32_u24_e32 v3, 0x110, v61
	v_add3_u32 v234, v2, v3, v6
	v_add_u32_e32 v0, 16, v0
	v_add_u32_e32 v1, 0x100, v1
	v_and_b32_e32 v61, 63, v0
	v_or_b32_e32 v11, s26, v61
	v_mov_b64_e32 v[2:3], s[24:25]
	s_movk_i32 s82, 0x1400
	s_mul_i32 s28, s27, 0x1400
	v_mad_u64_u32 v[2:3], s[82:83], v11, s82, v[2:3]
	v_add_u32_e32 v3, s28, v3
	v_and_b32_e32 v14, 0xfffffc00, v1
	v_lshl_add_u64 v[2:3], v[2:3], 0, v[14:15]
	s_lshl_b32 s28, s97, 1
	v_lshl_add_u64 v[2:3], v[2:3], 0, s[28:29]
	v_mov_b32_e32 v11, v15
	v_lshl_add_u64 v[2:3], v[2:3], 0, v[10:11]
	global_load_dwordx4 v[190:193], v[2:3], off
	v_lshrrev_b32_e32 v60, 10, v1
	v_mov_b32_e32 v2, s0
	s_movk_i32 s82, 0x4400
	v_mad_u32_u24 v2, v60, s82, v2
	v_mul_u32_u24_e32 v3, 0x110, v61
	v_add3_u32 v235, v2, v3, v6
	v_add_u32_e32 v0, 16, v0
	v_add_u32_e32 v1, 0x100, v1
	v_and_b32_e32 v61, 63, v0
	v_or_b32_e32 v11, s26, v61
	v_mov_b64_e32 v[2:3], s[24:25]
	s_movk_i32 s82, 0x1400
	s_mul_i32 s28, s27, 0x1400
	v_mad_u64_u32 v[2:3], s[82:83], v11, s82, v[2:3]
	v_add_u32_e32 v3, s28, v3
	v_and_b32_e32 v14, 0xfffffc00, v1
	v_lshl_add_u64 v[2:3], v[2:3], 0, v[14:15]
	s_lshl_b32 s28, s97, 1
	v_lshl_add_u64 v[2:3], v[2:3], 0, s[28:29]
	v_mov_b32_e32 v11, v15
	v_lshl_add_u64 v[2:3], v[2:3], 0, v[10:11]
	global_load_dwordx4 v[194:197], v[2:3], off
	v_lshrrev_b32_e32 v60, 10, v1
	v_mov_b32_e32 v2, s0
	s_movk_i32 s82, 0x4400
	v_mad_u32_u24 v2, v60, s82, v2
	v_mul_u32_u24_e32 v3, 0x110, v61
	v_add3_u32 v236, v2, v3, v6
	v_add_u32_e32 v0, 16, v0
	v_add_u32_e32 v1, 0x100, v1
	v_and_b32_e32 v61, 63, v0
	v_or_b32_e32 v11, s26, v61
	v_mov_b64_e32 v[2:3], s[24:25]
	s_movk_i32 s82, 0x1400
	s_mul_i32 s28, s27, 0x1400
	v_mad_u64_u32 v[2:3], s[82:83], v11, s82, v[2:3]
	v_add_u32_e32 v3, s28, v3
	v_and_b32_e32 v14, 0xfffffc00, v1
	v_lshl_add_u64 v[2:3], v[2:3], 0, v[14:15]
	s_lshl_b32 s28, s97, 1
	v_lshl_add_u64 v[2:3], v[2:3], 0, s[28:29]
	v_mov_b32_e32 v11, v15
	v_lshl_add_u64 v[2:3], v[2:3], 0, v[10:11]
	global_load_dwordx4 v[198:201], v[2:3], off
	v_lshrrev_b32_e32 v60, 10, v1
	v_mov_b32_e32 v2, s0
	s_movk_i32 s82, 0x4400
	v_mad_u32_u24 v2, v60, s82, v2
	v_mul_u32_u24_e32 v3, 0x110, v61
	v_add3_u32 v237, v2, v3, v6
	v_add_u32_e32 v0, 16, v0
	v_add_u32_e32 v1, 0x100, v1
	v_and_b32_e32 v61, 63, v0
	v_or_b32_e32 v11, s26, v61
	v_mov_b64_e32 v[2:3], s[24:25]
	s_movk_i32 s82, 0x1400
	s_mul_i32 s28, s27, 0x1400
	v_mad_u64_u32 v[2:3], s[82:83], v11, s82, v[2:3]
	v_add_u32_e32 v3, s28, v3
	v_and_b32_e32 v14, 0xfffffc00, v1
	v_lshl_add_u64 v[2:3], v[2:3], 0, v[14:15]
	s_lshl_b32 s28, s97, 1
	v_lshl_add_u64 v[2:3], v[2:3], 0, s[28:29]
	v_mov_b32_e32 v11, v15
	v_lshl_add_u64 v[2:3], v[2:3], 0, v[10:11]
	global_load_dwordx4 v[202:205], v[2:3], off
	v_lshrrev_b32_e32 v60, 10, v1
	v_mov_b32_e32 v2, s0
	s_movk_i32 s82, 0x4400
	v_mad_u32_u24 v2, v60, s82, v2
	v_mul_u32_u24_e32 v3, 0x110, v61
	v_add3_u32 v238, v2, v3, v6
	v_add_u32_e32 v0, 16, v0
	v_add_u32_e32 v1, 0x100, v1
	v_and_b32_e32 v61, 63, v0
	v_or_b32_e32 v11, s26, v61
	v_mov_b64_e32 v[2:3], s[24:25]
	s_movk_i32 s82, 0x1400
	s_mul_i32 s28, s27, 0x1400
	v_mad_u64_u32 v[2:3], s[82:83], v11, s82, v[2:3]
	v_add_u32_e32 v3, s28, v3
	v_and_b32_e32 v14, 0xfffffc00, v1
	v_lshl_add_u64 v[2:3], v[2:3], 0, v[14:15]
	s_lshl_b32 s28, s97, 1
	v_lshl_add_u64 v[2:3], v[2:3], 0, s[28:29]
	v_mov_b32_e32 v11, v15
	v_lshl_add_u64 v[2:3], v[2:3], 0, v[10:11]
	global_load_dwordx4 v[206:209], v[2:3], off
	v_lshrrev_b32_e32 v60, 10, v1
	v_mov_b32_e32 v2, s0
	s_movk_i32 s82, 0x4400
	v_mad_u32_u24 v2, v60, s82, v2
	v_mul_u32_u24_e32 v3, 0x110, v61
	v_add3_u32 v239, v2, v3, v6
	v_add_u32_e32 v0, 16, v0
	v_add_u32_e32 v1, 0x100, v1
	v_and_b32_e32 v61, 63, v0
	v_or_b32_e32 v11, s26, v61
	v_mov_b64_e32 v[2:3], s[24:25]
	s_movk_i32 s82, 0x1400
	s_mul_i32 s28, s27, 0x1400
	v_mad_u64_u32 v[2:3], s[82:83], v11, s82, v[2:3]
	v_add_u32_e32 v3, s28, v3
	v_and_b32_e32 v14, 0xfffffc00, v1
	v_lshl_add_u64 v[2:3], v[2:3], 0, v[14:15]
	s_lshl_b32 s28, s97, 1
	v_lshl_add_u64 v[2:3], v[2:3], 0, s[28:29]
	v_mov_b32_e32 v11, v15
	v_lshl_add_u64 v[2:3], v[2:3], 0, v[10:11]
	global_load_dwordx4 v[210:213], v[2:3], off
	v_lshrrev_b32_e32 v60, 10, v1
	v_mov_b32_e32 v2, s0
	s_movk_i32 s82, 0x4400
	v_mad_u32_u24 v2, v60, s82, v2
	v_mul_u32_u24_e32 v3, 0x110, v61
	v_add3_u32 v240, v2, v3, v6
	v_add_u32_e32 v0, 16, v0
	v_add_u32_e32 v1, 0x100, v1
	v_and_b32_e32 v61, 63, v0
	v_or_b32_e32 v11, s26, v61
	v_mov_b64_e32 v[2:3], s[24:25]
	s_movk_i32 s82, 0x1400
	s_mul_i32 s28, s27, 0x1400
	v_mad_u64_u32 v[2:3], s[82:83], v11, s82, v[2:3]
	v_add_u32_e32 v3, s28, v3
	v_and_b32_e32 v14, 0xfffffc00, v1
	v_lshl_add_u64 v[2:3], v[2:3], 0, v[14:15]
	s_lshl_b32 s28, s97, 1
	v_lshl_add_u64 v[2:3], v[2:3], 0, s[28:29]
	v_mov_b32_e32 v11, v15
; #define LAS __attribute__((address_space(3)))
; template <int NW> DI void dn1_unit(const Params& P, const Frame& F, int cidx) {
;     ...
;     for (int id = F.tid; id < 3072; id += NT) { const int which = id >> 10, rem = id & 1023, row = rem >> 4, ch = rem & 15;
;         *(LAS u32x4*)(Qs + which * 17408 + row * 272 + ch * 16) = *(const u32x4*)(ZC + (r0 + row) * 2560 + which * 512 + h * 128 + ch * 8); }
;     if (F.tid < 64) { bts[F.tid] = GD[(r0 + F.tid) * 16 + h]; const float gc = wave_incl_sum(GD[(r0 + F.tid) * 16 + 4 + h], lane); gcs[F.tid] = gc;
;         if (lane == 63) ((float*)(ws + WS_DNGL))[cidx] = __expf(gc); }
	v_lshl_add_u64 v[2:3], v[2:3], 0, v[10:11]
	global_load_dwordx4 v[214:217], v[2:3], off
	v_lshrrev_b32_e32 v60, 10, v1
	v_mov_b32_e32 v2, s0
	s_movk_i32 s82, 0x4400
	v_mad_u32_u24 v2, v60, s82, v2
	v_mul_u32_u24_e32 v3, 0x110, v61
	v_add3_u32 v241, v2, v3, v6
	v_add_u32_e32 v0, 16, v0
	v_add_u32_e32 v1, 0x100, v1
	v_and_b32_e32 v61, 63, v0
	v_or_b32_e32 v11, s26, v61
	v_mov_b64_e32 v[2:3], s[24:25]
	s_movk_i32 s82, 0x1400
	s_mul_i32 s28, s27, 0x1400
	v_mad_u64_u32 v[2:3], s[82:83], v11, s82, v[2:3]
	v_add_u32_e32 v3, s28, v3
	v_and_b32_e32 v14, 0xfffffc00, v1
	v_lshl_add_u64 v[2:3], v[2:3], 0, v[14:15]
	s_lshl_b32 s28, s97, 1
	v_lshl_add_u64 v[2:3], v[2:3], 0, s[28:29]
	v_mov_b32_e32 v11, v15
	v_lshl_add_u64 v[2:3], v[2:3], 0, v[10:11]
	global_load_dwordx4 v[218:221], v[2:3], off
	v_lshrrev_b32_e32 v60, 10, v1
	v_mov_b32_e32 v2, s0
	s_movk_i32 s82, 0x4400
	v_mad_u32_u24 v2, v60, s82, v2
	v_mul_u32_u24_e32 v3, 0x110, v61
	v_add3_u32 v242, v2, v3, v6
	v_add_u32_e32 v0, 16, v0
	v_add_u32_e32 v1, 0x100, v1
	v_and_b32_e32 v61, 63, v0
	v_or_b32_e32 v11, s26, v61
	v_mov_b64_e32 v[2:3], s[24:25]
	s_movk_i32 s82, 0x1400
	s_mul_i32 s28, s27, 0x1400
	v_mad_u64_u32 v[2:3], s[82:83], v11, s82, v[2:3]
	v_add_u32_e32 v3, s28, v3
	v_and_b32_e32 v14, 0xfffffc00, v1
	v_lshl_add_u64 v[2:3], v[2:3], 0, v[14:15]
	s_lshl_b32 s28, s97, 1
	v_lshl_add_u64 v[2:3], v[2:3], 0, s[28:29]
	v_mov_b32_e32 v11, v15
	v_lshl_add_u64 v[2:3], v[2:3], 0, v[10:11]
	global_load_dwordx4 v[222:225], v[2:3], off
	v_lshrrev_b32_e32 v60, 10, v1
	v_mov_b32_e32 v2, s0
	s_movk_i32 s82, 0x4400
	v_mad_u32_u24 v2, v60, s82, v2
	v_mul_u32_u24_e32 v3, 0x110, v61
	v_add3_u32 v243, v2, v3, v6
	v_add_u32_e32 v0, 16, v0
	v_add_u32_e32 v1, 0x100, v1
	v_and_b32_e32 v61, 63, v0
	v_or_b32_e32 v11, s26, v61
	v_mov_b64_e32 v[2:3], s[24:25]
	s_movk_i32 s82, 0x1400
	s_mul_i32 s28, s27, 0x1400
	v_mad_u64_u32 v[2:3], s[82:83], v11, s82, v[2:3]
	v_add_u32_e32 v3, s28, v3
	v_and_b32_e32 v14, 0xfffffc00, v1
	v_lshl_add_u64 v[2:3], v[2:3], 0, v[14:15]
	s_lshl_b32 s28, s97, 1
	v_lshl_add_u64 v[2:3], v[2:3], 0, s[28:29]
	v_mov_b32_e32 v11, v15
	v_lshl_add_u64 v[2:3], v[2:3], 0, v[10:11]
	global_load_dwordx4 v[226:229], v[2:3], off
	v_lshrrev_b32_e32 v60, 10, v1
	v_mov_b32_e32 v2, s0
	s_movk_i32 s82, 0x4400
	v_mad_u32_u24 v2, v60, s82, v2
	v_mul_u32_u24_e32 v3, 0x110, v61
	v_add3_u32 v244, v2, v3, v6
	v_add_u32_e32 v0, 16, v0
	v_add_u32_e32 v1, 0x100, v1
	v_and_b32_e32 v61, 63, v0
	v_or_b32_e32 v11, s26, v61
	v_mov_b64_e32 v[2:3], s[24:25]
	s_movk_i32 s82, 0x1400
	s_mul_i32 s28, s27, 0x1400
	v_mad_u64_u32 v[2:3], s[82:83], v11, s82, v[2:3]
	v_add_u32_e32 v3, s28, v3
	v_and_b32_e32 v14, 0xfffffc00, v1
	v_lshl_add_u64 v[2:3], v[2:3], 0, v[14:15]
	s_lshl_b32 s28, s97, 1
	v_lshl_add_u64 v[2:3], v[2:3], 0, s[28:29]
	v_mov_b32_e32 v11, v15
	v_lshl_add_u64 v[2:3], v[2:3], 0, v[10:11]
	global_load_dwordx4 v[230:233], v[2:3], off
	v_lshrrev_b32_e32 v60, 10, v1
	v_mov_b32_e32 v2, s0
	s_movk_i32 s82, 0x4400
	v_mad_u32_u24 v2, v60, s82, v2
	v_mul_u32_u24_e32 v3, 0x110, v61
	v_add3_u32 v245, v2, v3, v6
	s_waitcnt vmcnt(11)
	ds_write_b128 v234, v[186:189] offset:16896
	s_waitcnt vmcnt(10)
	ds_write_b128 v235, v[190:193] offset:16896
	s_waitcnt vmcnt(9)
	ds_write_b128 v236, v[194:197] offset:16896
	s_waitcnt vmcnt(8)
	ds_write_b128 v237, v[198:201] offset:16896
	s_waitcnt vmcnt(7)
	ds_write_b128 v238, v[202:205] offset:16896
	s_waitcnt vmcnt(6)
	ds_write_b128 v239, v[206:209] offset:16896
	s_waitcnt vmcnt(5)
	ds_write_b128 v240, v[210:213] offset:16896
	s_waitcnt vmcnt(4)
	ds_write_b128 v241, v[214:217] offset:16896
	s_waitcnt vmcnt(3)
	ds_write_b128 v242, v[218:221] offset:16896
	s_waitcnt vmcnt(2)
	ds_write_b128 v243, v[222:225] offset:16896
	s_waitcnt vmcnt(1)
	ds_write_b128 v244, v[226:229] offset:16896
	s_waitcnt vmcnt(0)
	ds_write_b128 v245, v[230:233] offset:16896
	s_or_b64 exec, exec, s[46:47]
	s_lshl_b32 s96, s49, 5
	s_or_b32 s46, s96, s3
	s_and_saveexec_b64 s[82:83], s[4:5]
	s_cbranch_execz .LBB0_1954
	s_lshl_b32 s48, s48, 2
	s_mov_b32 s49, s29
	v_lshl_add_u64 v[0:1], v[8:9], 0, s[48:49]
	global_load_dword v2, v[0:1], off offset:16
	s_nop 0
	global_load_dword v1, v[0:1], off
	v_readlane_b32 s48, v255, 0
	v_readlane_b32 s49, v255, 1
	s_waitcnt vmcnt(1)
	ds_bpermute_b32 v0, v62, v2
	s_waitcnt lgkmcnt(0)
	v_add_f32_e32 v0, v2, v0
	v_cndmask_b32_e64 v0, v0, v2, s[6:7]
	ds_bpermute_b32 v2, v63, v0
	s_waitcnt lgkmcnt(0)
	v_add_f32_e32 v2, v0, v2
	v_cndmask_b32_e64 v0, v2, v0, s[8:9]
	ds_bpermute_b32 v2, v64, v0
	s_waitcnt lgkmcnt(0)
	v_add_f32_e32 v2, v0, v2
	v_cndmask_b32_e64 v0, v2, v0, s[10:11]
	ds_bpermute_b32 v2, v65, v0
	s_waitcnt lgkmcnt(0)
	v_add_f32_e32 v2, v0, v2
	v_cndmask_b32_e64 v0, v2, v0, s[12:13]
	ds_bpermute_b32 v2, v66, v0
	s_waitcnt lgkmcnt(0)
	v_add_f32_e32 v2, v0, v2
	v_cndmask_b32_e64 v2, v2, v0, s[14:15]
	ds_bpermute_b32 v0, v67, v2
	s_waitcnt lgkmcnt(0)
	v_add_f32_e32 v0, v2, v0
	v_cndmask_b32_e64 v2, v0, v2, s[16:17]
	s_waitcnt vmcnt(0)
	ds_write2st64_b32 v72, v2, v1 offset0:64 offset1:65
	s_and_b64 exec, exec, s[48:49]
	s_cbranch_execz .LBB0_1954
	v_mul_f32_e32 v0, 0x3fb8aa3b, v0
	s_ashr_i32 s47, s46, 31
	v_exp_f32_e32 v0, v0
	s_lshl_b64 s[48:49], s[46:47], 2
	v_readlane_b32 s47, v255, 34
	s_add_u32 s48, s47, s48
	v_readlane_b32 s47, v255, 36
	s_addc_u32 s49, s47, s49
	global_store_dword v15, v0, s[48:49]
